# v52 + 6 s_nop so every later instruction keeps the byte phase it has in v44 (code placement)
# speedup vs baseline: 1.0032x; 1.0032x over previous
; __device__ __forceinline__ void first_norm_row(const float* xrow, const float* g, bf16* urow, bf16* hrow, int lane) {
;     const f32x4* xp = (const f32x4*)xrow; const f32x4* gp = (const f32x4*)g;
;     f32x4 v[4] = {xp[2 * lane], xp[2 * lane + 1], xp[128 + 2 * lane], xp[128 + 2 * lane + 1]};
; __device__ __forceinline__ void prologue(const Ctx& C, const In& I, unsigned char* ws, bf16* hs0) {
;     ...
;     if (C.G == 256) { const int mb = 2048 * (C.bx & 7) + 64 * (C.bx >> 3) + 8 * C.wave;
;         for (int m = mb; m < mb + 8; ++m) first_norm_row(I.x + (size_t)m * D, I.norm_g, U + (size_t)m * D, hs0 + (size_t)m * D, C.lane); }
.LBB0_89:
	s_andn2_b64 vcc, exec, s[0:1]
	s_cbranch_vccnz .LBB0_92
	s_lshl_b32 s0, s18, 11
	s_and_b32 s1, s0, 0x3800
	s_and_b32 s0, s18, 0x1ffffff8
	s_add_i32 s0, s19, s0
	s_lshl_b32 s4, s18, 3
	s_lshl_b32 s0, s0, 3
	s_andn2_b32 s4, s4, 63
	s_add_i32 s0, s0, s1
	s_add_i32 s1, s1, s4
	s_lshl_b32 s4, s19, 3
	s_add_i32 s1, s1, s4
	s_add_i32 s9, s1, -1
	s_ashr_i32 s1, s0, 31
	s_or_b32 s8, s0, 7
	s_lshl_b64 s[4:5], s[0:1], 11
	s_add_u32 s2, s2, s4
	v_readlane_b32 s12, v253, 16
	s_addc_u32 s3, s3, s5
	v_readlane_b32 s26, v253, 30
	v_readlane_b32 s27, v253, 31
	s_add_u32 s4, s26, s4
	v_readlane_b32 s36, v253, 0
	s_addc_u32 s5, s27, s5
	s_lshl_b64 s[0:1], s[0:1], 12
	v_readlane_b32 s37, v253, 1
	s_add_u32 s0, s36, s0
	v_lshlrev_b32_e32 v2, 5, v1
	v_mov_b32_e32 v3, 0
	v_readlane_b32 s38, v253, 2
	v_readlane_b32 s39, v253, 3
	s_addc_u32 s1, s37, s1
	v_lshlrev_b32_e32 v20, 4, v1
	v_lshl_add_u64 v[18:19], s[38:39], 0, v[2:3]
	v_mov_b32_e32 v21, v3
	v_lshl_add_u64 v[22:23], s[0:1], 0, v[2:3]
	v_lshlrev_b32_e32 v64, 2, v2
	v_mov_b32_e32 v65, 0
	v_lshl_add_u64 v[64:65], s[0:1], 0, v[64:65]
	s_mov_b64 s[6:7], 0x2000
	s_mov_b64 s[10:11], 0x4000
	global_load_dword v72, v[64:65], off
	v_lshl_add_u64 v[66:67], v[64:65], 0, s[6:7]
	v_lshl_add_u64 v[68:69], v[64:65], 0, s[10:11]
	global_load_dword v73, v[66:67], off
	global_load_dword v74, v[68:69], off
	v_lshl_add_u64 v[70:71], v[68:69], 0, s[6:7]
	global_load_dword v75, v[70:71], off
	s_nop 0
	s_nop 0
	s_nop 0
	s_nop 0
	s_nop 0
	s_nop 0
	v_mov_b32_e32 v1, 0x358637bd
	s_mov_b32 s10, 0xf800000
	v_mov_b32_e32 v24, 0x260
	s_brev_b32 s11, 64
	s_mov_b32 s12, 0xb000000
	s_mov_b64 s[6:7], 0x1000
	v_readlane_b32 s40, v253, 4
	v_readlane_b32 s41, v253, 5
	v_readlane_b32 s42, v253, 6
	v_readlane_b32 s43, v253, 7
	v_readlane_b32 s44, v253, 8
	v_readlane_b32 s45, v253, 9
	v_readlane_b32 s46, v253, 10
	v_readlane_b32 s47, v253, 11
	v_readlane_b32 s48, v253, 12
	v_readlane_b32 s49, v253, 13
	v_readlane_b32 s50, v253, 14
	v_readlane_b32 s51, v253, 15
	v_readlane_b32 s13, v253, 17
	v_readlane_b32 s14, v253, 18
	v_readlane_b32 s15, v253, 19
	v_readlane_b32 s16, v253, 20
	v_readlane_b32 s17, v253, 21
	v_readlane_b32 s18, v253, 22
	v_readlane_b32 s19, v253, 23
	v_readlane_b32 s20, v253, 24
	v_readlane_b32 s21, v253, 25
	v_readlane_b32 s22, v253, 26
	v_readlane_b32 s23, v253, 27
	v_readlane_b32 s24, v253, 28
	v_readlane_b32 s25, v253, 29
